# v048 + P13 first K-fragment read of each tile issued right behind the tile barrier
# baseline (speedup 1.0000x reference)
.LBB0_2751:
	v_add_u32_e32 v179, s39, v151
	v_add_u32_e32 v225, v179, v155
	v_add_u32_e32 v224, v179, v181
	v_add_u32_e32 v223, v179, v219
	s_waitcnt lgkmcnt(0)
	v_lshrrev_b32_e32 v82, v163, v226
	v_bfe_i32 v83, v82, 26, 1
	v_bitop3_b32 v96, v16, s28, v83 bitop3:0xe4
	v_bfe_i32 v83, v82, 25, 1
	v_bitop3_b32 v95, v13, s28, v83 bitop3:0xe4
	v_bfe_i32 v83, v82, 24, 1
	v_bitop3_b32 v94, v14, s28, v83 bitop3:0xe4
	v_bfe_i32 v83, v82, 19, 1
	v_bitop3_b32 v93, v11, s28, v83 bitop3:0xe4
	v_bfe_i32 v83, v82, 18, 1
	v_bitop3_b32 v92, v12, s28, v83 bitop3:0xe4
	v_bfe_i32 v83, v82, 17, 1
	v_add_u32_e32 v226, v179, v153
	v_bitop3_b32 v91, v9, s28, v83 bitop3:0xe4
	v_bfe_i32 v83, v82, 16, 1
	v_bitop3_b32 v90, v10, s28, v83 bitop3:0xe4
	v_bfe_i32 v83, v82, 11, 1
	v_bitop3_b32 v89, v7, s28, v83 bitop3:0xe4
	v_bfe_i32 v83, v82, 10, 1
	v_bitop3_b32 v88, v8, s28, v83 bitop3:0xe4
	v_bfe_i32 v83, v82, 9, 1
	v_bitop3_b32 v87, v5, s28, v83 bitop3:0xe4
	v_bfe_i32 v83, v82, 8, 1
	v_bitop3_b32 v86, v6, s28, v83 bitop3:0xe4
	v_bfe_i32 v83, v82, 3, 1
	v_bfe_i32 v84, v82, 27, 1
	v_bitop3_b32 v85, v3, s28, v83 bitop3:0xe4
	v_bfe_i32 v83, v82, 2, 1
	v_bitop3_b32 v97, v15, s28, v84 bitop3:0xe4
	v_bitop3_b32 v84, v4, s28, v83 bitop3:0xe4
	v_bfe_i32 v83, v82, 1, 1
	v_bfe_i32 v82, v82, 0, 1
	v_bitop3_b32 v83, v1, s28, v83 bitop3:0xe4
	v_bitop3_b32 v82, v2, s28, v82 bitop3:0xe4
	v_add_u32_e32 v179, s39, v17
	s_add_i32 s14, s37, 1
	s_waitcnt lgkmcnt(0)
	v_mfma_f32_32x32x16_bf16 v[98:113], v[186:189], v[114:117], v[82:97]
	s_cmp_lg_u32 s37, 2
	s_cselect_b32 s37, s14, 0
	s_add_u32 s0, s0, 0x4000
	s_addc_u32 s1, s1, 0
	s_add_i32 s38, s38, 1
	s_cmp_eq_u32 s36, s0
	v_add_u32_e32 v146, 8, v146
	v_mfma_f32_32x32x16_bf16 v[82:97], v[186:189], v[130:133], v[82:97]
	ds_read_b128 v[186:189], v225
	s_waitcnt lgkmcnt(0)
	v_mfma_f32_32x32x16_bf16 v[98:113], v[186:189], v[118:121], v[98:113]
	v_mfma_f32_32x32x16_bf16 v[82:97], v[186:189], v[134:137], v[82:97]
	ds_read_b128 v[186:189], v224
	s_waitcnt lgkmcnt(0)
	v_mfma_f32_32x32x16_bf16 v[98:113], v[186:189], v[122:125], v[98:113]
	v_mfma_f32_32x32x16_bf16 v[82:97], v[186:189], v[138:141], v[82:97]
	ds_read_b128 v[186:189], v223
	s_waitcnt lgkmcnt(0)
	v_mfma_f32_32x32x16_bf16 v[98:113], v[186:189], v[126:129], v[98:113]
	v_mfma_f32_32x32x16_bf16 v[82:97], v[186:189], v[142:145], v[82:97]
	s_nop 10
	v_exp_f32_e32 v190, v98
	v_exp_f32_e32 v191, v99
	v_exp_f32_e32 v192, v100
	v_exp_f32_e32 v193, v101
	s_nop 0
	ds_read_b64_tr_b16 v[98:99], v179 offset:49152
	ds_read_b64_tr_b16 v[100:101], v179 offset:50176
	v_exp_f32_e32 v188, v102
	v_exp_f32_e32 v189, v103
	v_exp_f32_e32 v186, v104
	v_exp_f32_e32 v187, v105
	ds_read_b64_tr_b16 v[212:213], v179 offset:50688
	ds_read_b64_tr_b16 v[210:211], v179 offset:49664
	v_exp_f32_e32 v204, v82
	v_exp_f32_e32 v205, v83
	v_exp_f32_e32 v208, v84
	v_exp_f32_e32 v209, v85
	v_exp_f32_e32 v200, v86
	v_exp_f32_e32 v201, v87
	v_exp_f32_e32 v196, v88
	v_exp_f32_e32 v197, v89
	v_cvt_pk_bf16_f32 v102, v190, v191
	v_cvt_pk_bf16_f32 v103, v192, v193
	v_cvt_pk_bf16_f32 v104, v188, v189
	v_cvt_pk_bf16_f32 v105, v186, v187
	v_cvt_pk_bf16_f32 v82, v204, v205
	v_cvt_pk_bf16_f32 v83, v208, v209
	s_waitcnt lgkmcnt(2)
	v_mfma_f32_32x32x16_bf16 v[66:81], v[98:101], v[102:105], v[66:81]
	v_cvt_pk_bf16_f32 v84, v200, v201
	v_cvt_pk_bf16_f32 v85, v196, v197
	v_exp_f32_e32 v206, v106
	v_exp_f32_e32 v207, v107
	v_exp_f32_e32 v202, v108
	v_exp_f32_e32 v203, v109
	v_exp_f32_e32 v198, v110
	s_waitcnt lgkmcnt(0)
	v_mfma_f32_32x32x16_bf16 v[50:65], v[210:213], v[102:105], v[50:65]
	v_exp_f32_e32 v199, v111
	v_exp_f32_e32 v194, v112
	v_exp_f32_e32 v195, v113
	v_exp_f32_e32 v216, v90
	v_exp_f32_e32 v217, v91
	v_exp_f32_e32 v214, v92
	v_exp_f32_e32 v215, v93
	v_mfma_f32_32x32x16_bf16 v[34:49], v[98:101], v[82:85], v[34:49]
	v_cvt_pk_bf16_f32 v86, v206, v207
	v_cvt_pk_bf16_f32 v87, v202, v203
	v_cvt_pk_bf16_f32 v88, v198, v199
	v_cvt_pk_bf16_f32 v89, v194, v195
	v_mfma_f32_32x32x16_bf16 v[18:33], v[210:213], v[82:85], v[18:33]
	ds_read_b64_tr_b16 v[82:83], v179 offset:51200
	ds_read_b64_tr_b16 v[84:85], v179 offset:52224
	ds_read_b64_tr_b16 v[100:101], v179 offset:52736
	ds_read_b64_tr_b16 v[98:99], v179 offset:51712
	v_exp_f32_e32 v212, v94
	v_exp_f32_e32 v213, v95
	v_exp_f32_e32 v210, v96
	v_exp_f32_e32 v211, v97
	s_waitcnt lgkmcnt(2)
	v_mfma_f32_32x32x16_bf16 v[66:81], v[82:85], v[86:89], v[66:81]
	s_waitcnt lgkmcnt(0)
	v_mfma_f32_32x32x16_bf16 v[50:65], v[98:101], v[86:89], v[50:65]
	v_cvt_pk_bf16_f32 v86, v216, v217
	v_cvt_pk_bf16_f32 v87, v214, v215
	v_cvt_pk_bf16_f32 v88, v212, v213
	v_cvt_pk_bf16_f32 v89, v210, v211
	s_nop 1
	v_mfma_f32_32x32x16_bf16 v[34:49], v[82:85], v[86:89], v[34:49]
	v_lshrrev_b32_e32 v82, v163, v227
	v_bfe_i32 v83, v82, 26, 1
	v_bitop3_b32 v96, v16, s28, v83 bitop3:0xe4
	v_bfe_i32 v83, v82, 25, 1
	v_bitop3_b32 v95, v13, s28, v83 bitop3:0xe4
	v_bfe_i32 v83, v82, 24, 1
	v_bitop3_b32 v94, v14, s28, v83 bitop3:0xe4
	v_bfe_i32 v83, v82, 19, 1
	v_bitop3_b32 v93, v11, s28, v83 bitop3:0xe4
	v_bfe_i32 v83, v82, 18, 1
	v_bitop3_b32 v92, v12, s28, v83 bitop3:0xe4
	v_bfe_i32 v83, v82, 17, 1
	v_bitop3_b32 v91, v9, s28, v83 bitop3:0xe4
	v_bfe_i32 v83, v82, 16, 1
	ds_read_b128 v[226:229], v226 offset:4096
	v_bitop3_b32 v90, v10, s28, v83 bitop3:0xe4
	v_bfe_i32 v83, v82, 11, 1
	v_mfma_f32_32x32x16_bf16 v[18:33], v[98:101], v[86:89], v[18:33]
	v_bitop3_b32 v89, v7, s28, v83 bitop3:0xe4
	v_bfe_i32 v83, v82, 10, 1
	v_bitop3_b32 v88, v8, s28, v83 bitop3:0xe4
	v_bfe_i32 v83, v82, 9, 1
	v_bitop3_b32 v87, v5, s28, v83 bitop3:0xe4
	v_bfe_i32 v83, v82, 8, 1
	v_bitop3_b32 v86, v6, s28, v83 bitop3:0xe4
	v_bfe_i32 v83, v82, 3, 1
	v_bfe_i32 v84, v82, 27, 1
	v_bitop3_b32 v85, v3, s28, v83 bitop3:0xe4
	v_bfe_i32 v83, v82, 2, 1
	v_bitop3_b32 v97, v15, s28, v84 bitop3:0xe4
	v_bitop3_b32 v84, v4, s28, v83 bitop3:0xe4
	v_bfe_i32 v83, v82, 1, 1
	v_bfe_i32 v82, v82, 0, 1
	v_bitop3_b32 v83, v1, s28, v83 bitop3:0xe4
	v_bitop3_b32 v82, v2, s28, v82 bitop3:0xe4
	s_waitcnt lgkmcnt(0)
	s_nop 0
	v_mfma_f32_32x32x16_bf16 v[98:113], v[226:229], v[114:117], v[82:97]
	v_mfma_f32_32x32x16_bf16 v[82:97], v[226:229], v[130:133], v[82:97]
	ds_read_b128 v[226:229], v225 offset:4096
	s_waitcnt lgkmcnt(0)
	v_mfma_f32_32x32x16_bf16 v[98:113], v[226:229], v[118:121], v[98:113]
	v_mfma_f32_32x32x16_bf16 v[82:97], v[226:229], v[134:137], v[82:97]
	ds_read_b128 v[224:227], v224 offset:4096
	s_waitcnt lgkmcnt(0)
	v_mfma_f32_32x32x16_bf16 v[98:113], v[224:227], v[122:125], v[98:113]
	v_mfma_f32_32x32x16_bf16 v[82:97], v[224:227], v[138:141], v[82:97]
	ds_read_b128 v[224:227], v223 offset:4096
	s_waitcnt lgkmcnt(0)
	v_mfma_f32_32x32x16_bf16 v[98:113], v[224:227], v[126:129], v[98:113]
	v_mfma_f32_32x32x16_bf16 v[82:97], v[224:227], v[142:145], v[82:97]
	s_nop 10
	v_exp_f32_e32 v228, v98
	v_exp_f32_e32 v229, v99
	v_exp_f32_e32 v230, v100
	v_exp_f32_e32 v231, v101
	ds_read_b64_tr_b16 v[98:99], v179 offset:53248
	ds_read_b64_tr_b16 v[100:101], v179 offset:54272
	v_exp_f32_e32 v232, v102
	v_exp_f32_e32 v233, v103
	v_exp_f32_e32 v234, v104
	v_exp_f32_e32 v235, v105
	ds_read_b64_tr_b16 v[226:227], v179 offset:54784
	ds_read_b64_tr_b16 v[224:225], v179 offset:53760
	v_cvt_pk_bf16_f32 v102, v228, v229
	v_cvt_pk_bf16_f32 v103, v230, v231
	v_cvt_pk_bf16_f32 v104, v232, v233
	v_cvt_pk_bf16_f32 v105, v234, v235
	v_exp_f32_e32 v236, v86
	v_exp_f32_e32 v237, v87
	s_waitcnt lgkmcnt(2)
	v_mfma_f32_32x32x16_bf16 v[66:81], v[98:101], v[102:105], v[66:81]
	v_exp_f32_e32 v238, v88
	v_exp_f32_e32 v239, v89
	v_exp_f32_e32 v106, v106
	v_exp_f32_e32 v107, v107
	v_exp_f32_e32 v108, v108
	v_exp_f32_e32 v109, v109
	v_exp_f32_e32 v110, v110
	s_waitcnt lgkmcnt(0)
	v_mfma_f32_32x32x16_bf16 v[50:65], v[224:227], v[102:105], v[50:65]
	v_exp_f32_e32 v102, v82
	v_exp_f32_e32 v103, v83
	v_exp_f32_e32 v104, v84
	v_exp_f32_e32 v105, v85
	v_cvt_pk_bf16_f32 v84, v236, v237
	v_cvt_pk_bf16_f32 v82, v102, v103
	v_cvt_pk_bf16_f32 v85, v238, v239
	v_cvt_pk_bf16_f32 v83, v104, v105
	v_exp_f32_e32 v111, v111
	v_exp_f32_e32 v112, v112
	v_mfma_f32_32x32x16_bf16 v[34:49], v[98:101], v[82:85], v[34:49]
	v_exp_f32_e32 v113, v113
	v_exp_f32_e32 v90, v90
	v_exp_f32_e32 v91, v91
	v_exp_f32_e32 v92, v92
	v_exp_f32_e32 v93, v93
	v_exp_f32_e32 v94, v94
	v_exp_f32_e32 v95, v95
	v_mfma_f32_32x32x16_bf16 v[18:33], v[224:227], v[82:85], v[18:33]
	ds_read_b64_tr_b16 v[82:83], v179 offset:55296
	ds_read_b64_tr_b16 v[84:85], v179 offset:56320
	ds_read_b64_tr_b16 v[100:101], v179 offset:56832
	ds_read_b64_tr_b16 v[98:99], v179 offset:55808
	v_exp_f32_e32 v96, v96
	v_exp_f32_e32 v97, v97
	v_cvt_pk_bf16_f32 v86, v106, v107
	v_cvt_pk_bf16_f32 v87, v108, v109
	v_cvt_pk_bf16_f32 v88, v110, v111
	v_cvt_pk_bf16_f32 v89, v112, v113
	s_waitcnt lgkmcnt(2)
	s_nop 0
	v_mfma_f32_32x32x16_bf16 v[66:81], v[82:85], v[86:89], v[66:81]
	s_waitcnt lgkmcnt(0)
	v_mfma_f32_32x32x16_bf16 v[50:65], v[98:101], v[86:89], v[50:65]
	v_cvt_pk_bf16_f32 v86, v90, v91
	v_cvt_pk_bf16_f32 v87, v92, v93
	v_cvt_pk_bf16_f32 v88, v94, v95
	v_cvt_pk_bf16_f32 v89, v96, v97
	s_nop 1
	v_mfma_f32_32x32x16_bf16 v[34:49], v[82:85], v[86:89], v[34:49]
	v_add_f32_e64 v82, v190, 0
	v_add_f32_e64 v83, v191, 0
	v_add_f32_e64 v84, v228, 0
	v_add_f32_e64 v85, v229, 0
	v_add_f32_e64 v82, v192, v82
	v_add_f32_e64 v83, v193, v83
	v_pk_add_f32 v[84:85], v[230:231], v[84:85]
	v_pk_add_f32 v[82:83], v[188:189], v[82:83]
	v_pk_add_f32 v[84:85], v[232:233], v[84:85]
	v_pk_add_f32 v[82:83], v[186:187], v[82:83]
	v_mfma_f32_32x32x16_bf16 v[18:33], v[98:101], v[86:89], v[18:33]
	v_add_f32_e64 v86, v204, 0
	v_add_f32_e64 v87, v205, 0
	v_add_f32_e64 v88, v102, 0
	v_add_f32_e64 v89, v103, 0
	v_add_f32_e64 v86, v208, v86
	v_add_f32_e64 v87, v209, v87
	v_pk_add_f32 v[88:89], v[104:105], v[88:89]
	v_pk_add_f32 v[86:87], v[200:201], v[86:87]
	v_pk_add_f32 v[88:89], v[236:237], v[88:89]
	v_pk_add_f32 v[84:85], v[234:235], v[84:85]
	v_pk_add_f32 v[86:87], v[196:197], v[86:87]
	v_pk_add_f32 v[88:89], v[238:239], v[88:89]
	v_pk_add_f32 v[82:83], v[206:207], v[82:83]
	v_pk_add_f32 v[84:85], v[106:107], v[84:85]
	v_pk_add_f32 v[86:87], v[216:217], v[86:87]
	v_pk_add_f32 v[88:89], v[90:91], v[88:89]
	v_pk_add_f32 v[82:83], v[202:203], v[82:83]
	v_pk_add_f32 v[84:85], v[108:109], v[84:85]
	v_pk_add_f32 v[86:87], v[214:215], v[86:87]
	v_pk_add_f32 v[88:89], v[92:93], v[88:89]
	v_pk_add_f32 v[82:83], v[198:199], v[82:83]
	v_pk_add_f32 v[84:85], v[110:111], v[84:85]
	v_pk_add_f32 v[86:87], v[212:213], v[86:87]
	v_pk_add_f32 v[88:89], v[94:95], v[88:89]
	v_pk_add_f32 v[82:83], v[194:195], v[82:83]
	v_pk_add_f32 v[84:85], v[112:113], v[84:85]
	v_pk_add_f32 v[86:87], v[210:211], v[86:87]
	v_pk_add_f32 v[88:89], v[96:97], v[88:89]
	v_pk_add_f32 v[82:83], v[82:83], v[84:85]
	v_pk_add_f32 v[84:85], v[86:87], v[88:89]
	v_mov_b32_e32 v86, v82
	v_mov_b32_e32 v87, v84
	v_mov_b32_e32 v84, v83
	v_pk_add_f32 v[82:83], v[86:87], v[84:85]
	s_nop 0
	v_pk_add_f32 v[184:185], v[184:185], v[82:83]
	s_cbranch_scc1 .LBB0_2745

.LBB0_2756:
	s_barrier
	ds_read_b64 v[226:227], v146
	s_lshl_b32 s14, s37, 14
	v_add_u32_e32 v240, s14, v151
	v_add_u32_e32 v240, v240, v153
	ds_read_b128 v[186:189], v240
	s_cmp_le_u32 s38, s34
	s_mov_b64 s[14:15], -1
	s_cbranch_scc0 .LBB0_2758
	s_lshl_b32 s39, s37, 14
	s_add_i32 s14, s39, 0xffffc000
	s_cmp_lg_u32 s37, 0
	s_cselect_b32 s40, s14, 0x8000
	v_lshl_add_u64 v[82:83], v[182:183], 0, s[0:1]
	s_mov_b64 s[14:15], 0x39208000
	s_add_i32 s40, s22, s40
	v_lshl_add_u64 v[84:85], v[82:83], 0, s[14:15]
	s_mov_b32 m0, s40
	s_mov_b64 s[14:15], 0x39208080
	global_load_lds_dwordx4 v[84:85], off
	v_lshl_add_u64 v[82:83], v[82:83], 0, s[14:15]
	s_add_i32 m0, s40, 0x2000
	s_mov_b64 s[14:15], 0x3a208000
	global_load_lds_dwordx4 v[82:83], off
	v_lshl_add_u64 v[82:83], v[172:173], 0, s[0:1]
	v_lshl_add_u64 v[84:85], v[82:83], 0, s[14:15]
	s_add_i32 m0, s40, 0xc000
	v_lshl_add_u64 v[82:83], v[82:83], 0, s[12:13]
	global_load_lds_dwordx4 v[84:85], off
	s_add_i32 m0, s40, 0xe000
	s_mov_b64 s[14:15], 0
	global_load_lds_dwordx4 v[82:83], off
